# speedup vs baseline: 1.0153x; 1.0103x over previous
.LBB1_33:
	s_cmp_gt_u32 s43, 22
	s_cselect_b64 s[38:39], -1, 0
	s_xor_b32 s8, s12, 1
	v_cmp_eq_u32_e64 s[4:5], -1, v190
	v_mov_b32_e32 v156, v142
	v_mov_b32_e32 v157, v140
	s_mulk_i32 s8, 0x4200
	s_mov_b64 s[52:53], s[6:7]
	s_mov_b32 s45, 0
	s_barrier
	s_cmp_lg_u64 s[10:11], 0
	s_cbranch_scc1 .Lq_noearly
	global_load_dwordx4 v[140:143], v228, s[52:53] sc1
	global_load_dwordx4 v[144:147], v229, s[52:53] sc1
	global_load_dwordx4 v[148:151], v230, s[52:53] sc1
.Lq_noearly:
	v_mov_b32_e32 v152, 0x44800000
	v_add_u32_e32 v208, s8, v195
	v_lshl_add_u32 v155, v181, 1, v208
	v_cndmask_b32_e64 v152, v152, 0, s[4:5]
	v_fma_mixlo_f16 v153, v156, v152, 0
	v_fma_mixhi_f16 v153, v157, v152, 0
	s_cmp_lt_u32 s43, 23
	ds_write_b16 v155, v153
	ds_write_b16_d16_hi v155, v153 offset:8
	s_cbranch_scc1 .LBB1_35
	v_fma_mixlo_f16 v154, v156, v152, -v153 op_sel_hi:[0,0,1]
	v_fma_mixhi_f16 v154, v157, v152, -v153 op_sel:[0,0,1] op_sel_hi:[0,0,1]
	ds_write_b16 v155, v154 offset:8448
	ds_write_b16_d16_hi v155, v154 offset:8456
.LBB1_35:
	s_xor_b64 s[8:9], s[10:11], -1
	s_andn2_b64 vcc, exec, s[8:9]
	s_cbranch_vccnz .LBB1_44
	s_branch .Lq_wait

.Lq_wait:
	s_waitcnt vmcnt(2)
	v_cmp_eq_u32_e32 vcc, s44, v141
	v_cmp_eq_u32_e64 s[6:7], s44, v143
	s_waitcnt vmcnt(1)
	v_cmp_eq_u32_e64 s[8:9], s44, v145
	s_and_b64 s[6:7], vcc, s[6:7]
	v_cmp_eq_u32_e64 s[10:11], s44, v147
	s_and_b64 s[6:7], s[6:7], s[8:9]
	s_waitcnt vmcnt(0)
	v_cmp_eq_u32_e64 s[12:13], s44, v149
	s_and_b64 s[6:7], s[6:7], s[10:11]
	v_cmp_eq_u32_e64 s[14:15], s44, v151
	s_and_b64 s[6:7], s[6:7], s[12:13]
	s_and_b64 s[6:7], s[6:7], s[14:15]
	s_cmp_eq_u64 s[6:7], exec
	s_cbranch_scc1 .Lp8_got
	s_add_i32 s45, s45, 1
	s_and_b32 s6, s45, 0x3ff
	s_cmp_lg_u32 s6, 0
	s_cbranch_scc1 .LBB1_38
	s_cmp_lt_u32 s45, 0x80001
	s_cbranch_scc0 .Lp9_timeout
	global_load_dword v141, v167, s[22:23] offset:4 sc1
	s_waitcnt vmcnt(0)
	v_readfirstlane_b32 s6, v141
	s_cmp_eq_u32 s6, 0
	s_cbranch_scc1 .LBB1_38
